# v28_pad16
# baseline (speedup 1.0000x reference)
.Lp1_lds_1:
	v_mov_b32_e32 v72, v68
	s_nop 0
	ds_read2_b32 v[66:67], v72 offset1:68
	ds_read2_b32 v[68:69], v72 offset0:136 offset1:204
	s_waitcnt lgkmcnt(0)
	s_branch .Lp1_go_1
	s_nop 0
	s_nop 0
	s_nop 0
	s_nop 0
.Lp1_fast_1:
	s_add_i32 s84, s84, 1
	v_add_u32_e32 v162, 0x1100, v162
	v_add_u32_e32 v161, 0x1140, v161
	s_cmp_lg_u32 s56, 4
	v_add_u32_e32 v160, 0x1140, v160
	s_cbranch_scc0 .LBB1_125
	s_mov_b32 s59, s56
	s_mov_b64 s[54:55], -1
	s_lshl_b32 s96, s59, 4
	v_or_b32_e32 v164, s96, v131
	v_lshlrev_b32_e32 v163, 2, v164
	v_or_b32_e32 v66, s96, v130
	v_mul_u32_u24_e32 v165, s95, v66
	v_add3_u32 v68, v163, v165, s85
	v_accvgpr_read_b32 v66, a0
	v_accvgpr_read_b32 v67, a1
	v_accvgpr_read_b32 v68, a2
	v_accvgpr_read_b32 v69, a3

.Lp1_lds_2:
	v_mov_b32_e32 v8, v4
	s_nop 0
	ds_read2_b32 v[2:3], v8 offset1:68
	ds_read2_b32 v[4:5], v8 offset0:136 offset1:204
	s_waitcnt lgkmcnt(0)
	s_branch .Lp1_go_2
	s_nop 0
	s_nop 0
	s_nop 0
	s_nop 0
.Lp1_fast_2:
	s_add_i32 s94, s94, 1
	v_add_u32_e32 v145, 0x1100, v145
	v_add_u32_e32 v147, 0x1140, v147
	s_cmp_lg_u32 s56, 4
	v_add_u32_e32 v11, 0x1140, v11
	s_cbranch_scc0 .LBB1_246
	s_mov_b32 s59, s56
	s_mov_b64 s[52:53], -1
	s_lshl_b32 s97, s59, 4
	v_or_b32_e32 v14, s97, v131
	v_lshlrev_b32_e32 v13, 2, v14
	v_or_b32_e32 v2, s97, v130
	v_mul_u32_u24_e32 v15, s57, v2
	v_add3_u32 v4, v13, v15, s95
	v_accvgpr_read_b32 v2, a0
	v_accvgpr_read_b32 v3, a1
	v_accvgpr_read_b32 v4, a2
	v_accvgpr_read_b32 v5, a3

.Lp1_lds_3:
	v_mov_b32_e32 v8, v4
	s_nop 0
	ds_read2_b32 v[2:3], v8 offset1:68
	ds_read2_b32 v[4:5], v8 offset0:136 offset1:204
	s_waitcnt lgkmcnt(0)
	s_branch .Lp1_go_3
	s_nop 0
	s_nop 0
	s_nop 0
	s_nop 0
.Lp1_fast_3:
	s_add_i32 s68, s68, 1
	v_add_u32_e32 v40, 0x1100, v40
	v_add_u32_e32 v39, 0x1140, v39
	s_cmp_lg_u32 s52, 4
	v_add_u32_e32 v38, 0x1140, v38
	s_cbranch_scc0 .LBB1_316
	s_mov_b32 s79, s52
	s_mov_b64 s[52:53], -1
	s_lshl_b32 s80, s79, 4
	v_or_b32_e32 v42, s80, v19
	v_lshlrev_b32_e32 v41, 2, v42
	v_or_b32_e32 v2, s80, v18
	v_mul_u32_u24_e32 v44, s78, v2
	v_add3_u32 v4, v41, v44, s69
	v_accvgpr_read_b32 v2, a0
	v_accvgpr_read_b32 v3, a1
	v_accvgpr_read_b32 v4, a2
	v_accvgpr_read_b32 v5, a3

.Lp1_lds_4:
	v_mov_b32_e32 v6, v2
	s_nop 0
	ds_read2_b32 v[0:1], v6 offset1:68
	ds_read2_b32 v[2:3], v6 offset0:136 offset1:204
	s_waitcnt lgkmcnt(0)
	s_branch .Lp1_go_4
	s_nop 0
	s_nop 0
	s_nop 0
	s_nop 0
.Lp1_fast_4:
	s_add_i32 s65, s65, 1
	v_add_u32_e32 v30, 0x1100, v30
	v_add_u32_e32 v32, 0x1140, v32
	s_cmp_lg_u32 s52, 4
	v_add_u32_e32 v12, 0x1140, v12
	s_cbranch_scc0 .LBB1_357
	s_mov_b32 s74, s52
	s_mov_b64 s[52:53], -1
	s_lshl_b32 s75, s74, 4
	v_or_b32_e32 v34, s75, v19
	v_lshlrev_b32_e32 v14, 2, v34
	v_or_b32_e32 v0, s75, v18
	v_mul_u32_u24_e32 v35, s64, v0
	v_add3_u32 v2, v14, v35, s72
	v_accvgpr_read_b32 v0, a0
	v_accvgpr_read_b32 v1, a1
	v_accvgpr_read_b32 v2, a2
	v_accvgpr_read_b32 v3, a3
